# G6 epilogue: residual x loads (read last before the in-place update) marked nt
# baseline (speedup 1.0000x reference)
;     __device__ __forceinline__ void operator()(const f32x4 (&acc)[2][2][4][2], const Unit& u, int wr, int wc, int fr, int fq) const {
;         const int row0 = u.pm * BM + wr * 64 + fr, col0 = u.pn * BM + wc * 32 + 4 * fq;
; #pragma unroll
;         for (int ai = 0; ai < 2; ++ai) { f32x4 xv[4][2][2];
; #pragma unroll
;             for (int m = 0; m < 4; ++m) { const size_t off = (size_t)(row0 + ai * HALF + m * 16) * 1024 + col0;
; #pragma unroll
;                 for (int bj = 0; bj < 2; ++bj)
; #pragma unroll
;                     for (int n = 0; n < 2; ++n) xv[m][bj][n] = *(const f32x4*)(xin + off + bj * HALF + n * 16); }
; #pragma unroll
;             for (int m = 0; m < 4; ++m) asm volatile("" : "+v"(xv[m][0][0]), "+v"(xv[m][0][1]), "+v"(xv[m][1][0]), "+v"(xv[m][1][1]));
; #pragma unroll
;             for (int m = 0; m < 4; ++m) { const size_t off = (size_t)(row0 + ai * HALF + m * 16) * 1024 + col0;
; #pragma unroll
;                 for (int bj = 0; bj < 2; ++bj)
; #pragma unroll
;                     for (int n = 0; n < 2; ++n) *(f32x4*)(out + off + bj * HALF + n * 16) = xv[m][bj][n] + acc[ai][bj][m][n]; } }
.LBB0_2490:
	v_lshl_add_u32 v130, s18, 8, v174
	v_lshl_or_b32 v132, s19, 8, v176
	v_ashrrev_i32_e32 v131, 31, v130
	v_ashrrev_i32_e32 v133, 31, v132
	v_lshlrev_b64 v[168:169], 12, v[130:131]
	v_or_b32_e32 v134, 16, v130
	v_or_b32_e32 v136, 32, v130
	v_or_b32_e32 v130, 48, v130
	v_lshlrev_b64 v[164:165], 2, v[132:133]
	v_ashrrev_i32_e32 v135, 31, v134
	v_ashrrev_i32_e32 v137, 31, v136
	v_ashrrev_i32_e32 v131, 31, v130
	v_lshl_add_u64 v[166:167], s[4:5], 0, v[164:165]
	v_lshlrev_b64 v[214:215], 12, v[134:135]
	v_lshlrev_b64 v[172:173], 12, v[136:137]
	v_lshlrev_b64 v[170:171], 12, v[130:131]
	v_lshl_add_u64 v[132:133], v[166:167], 0, v[168:169]
	v_lshl_add_u64 v[134:135], v[166:167], 0, v[214:215]
	v_lshl_add_u64 v[136:137], v[166:167], 0, v[172:173]
	v_lshl_add_u64 v[150:151], v[166:167], 0, v[170:171]
	global_load_dwordx4 v[178:181], v[132:133], off offset:576 nt
	global_load_dwordx4 v[182:185], v[132:133], off offset:512 nt
	global_load_dwordx4 v[186:189], v[132:133], off offset:64 nt
	global_load_dwordx4 v[190:193], v[132:133], off nt
	global_load_dwordx4 v[194:197], v[134:135], off offset:576 nt
	global_load_dwordx4 v[198:201], v[134:135], off offset:512 nt
	global_load_dwordx4 v[202:205], v[134:135], off offset:64 nt
	global_load_dwordx4 v[206:209], v[134:135], off nt
	global_load_dwordx4 v[142:145], v[136:137], off offset:576 nt
	global_load_dwordx4 v[146:149], v[136:137], off offset:512 nt
	global_load_dwordx4 v[154:157], v[136:137], off offset:64 nt
	global_load_dwordx4 v[210:213], v[136:137], off nt
	global_load_dwordx4 v[130:133], v[150:151], off offset:576 nt
	s_nop 0
	global_load_dwordx4 v[134:137], v[150:151], off offset:512 nt
	global_load_dwordx4 v[138:141], v[150:151], off offset:64 nt
	s_nop 0
	global_load_dwordx4 v[150:153], v[150:151], off nt
	v_readlane_b32 s20, v252, 17
	v_readlane_b32 s21, v252, 18
	s_mov_b64 s[18:19], 0x80000
	s_andn2_b64 vcc, exec, s[0:1]
	s_waitcnt vmcnt(0)
	s_nop 0
	v_pk_add_f32 v[126:127], v[126:127], v[190:191]
	v_lshl_add_u64 v[190:191], s[20:21], 0, v[168:169]
	v_lshl_add_u64 v[190:191], v[190:191], 0, v[164:165]
	v_pk_add_f32 v[116:117], v[116:117], v[184:185]
	v_pk_add_f32 v[114:115], v[114:115], v[182:183]
	global_store_dwordx4 v[190:191], v[114:117], off offset:512
	v_pk_add_f32 v[100:101], v[100:101], v[200:201]
	v_pk_add_f32 v[98:99], v[98:99], v[198:199]
	v_lshl_add_u64 v[114:115], s[20:21], 0, v[214:215]
	v_lshl_add_u64 v[114:115], v[114:115], 0, v[164:165]
	global_store_dwordx4 v[114:115], v[98:101], off offset:512
	v_pk_add_f32 v[96:97], v[96:97], v[196:197]
	v_pk_add_f32 v[94:95], v[94:95], v[194:195]
	v_lshl_add_u64 v[98:99], s[20:21], 0, v[172:173]
	v_pk_add_f32 v[70:71], v[70:71], v[134:135]
	v_lshl_add_u64 v[134:135], v[168:169], 0, s[18:19]
	s_mov_b64 s[18:19], 0x90000
	global_store_dwordx4 v[114:115], v[94:97], off offset:576
	v_lshl_add_u64 v[98:99], v[98:99], 0, v[164:165]
	v_pk_add_f32 v[84:85], v[84:85], v[148:149]
	v_pk_add_f32 v[96:97], v[104:105], v[212:213]
	v_pk_add_f32 v[94:95], v[102:103], v[210:211]
	v_pk_add_f32 v[82:83], v[82:83], v[146:147]
	v_pk_add_f32 v[72:73], v[72:73], v[136:137]
	v_lshl_add_u64 v[136:137], v[168:169], 0, s[18:19]
	s_mov_b64 s[18:19], 0xa0000
	v_pk_add_f32 v[112:113], v[112:113], v[180:181]
	v_pk_add_f32 v[110:111], v[110:111], v[178:179]
	global_store_dwordx4 v[98:99], v[94:97], off
	global_store_dwordx4 v[98:99], v[82:85], off offset:512
	v_pk_add_f32 v[80:81], v[80:81], v[144:145]
	v_pk_add_f32 v[78:79], v[78:79], v[142:143]
	v_lshl_add_u64 v[82:83], s[20:21], 0, v[170:171]
	v_lshl_add_u64 v[96:97], v[168:169], 0, s[18:19]
	s_mov_b64 s[18:19], 0xb0000
	v_pk_add_f32 v[128:129], v[128:129], v[192:193]
	v_pk_add_f32 v[124:125], v[124:125], v[188:189]
	v_pk_add_f32 v[122:123], v[122:123], v[186:187]
	global_store_dwordx4 v[190:191], v[110:113], off offset:576
	v_pk_add_f32 v[108:109], v[108:109], v[204:205]
	v_pk_add_f32 v[106:107], v[106:107], v[202:203]
	v_pk_add_f32 v[112:113], v[120:121], v[208:209]
	v_pk_add_f32 v[110:111], v[118:119], v[206:207]
	v_pk_add_f32 v[92:93], v[92:93], v[156:157]
	v_pk_add_f32 v[90:91], v[90:91], v[154:155]
	global_store_dwordx4 v[98:99], v[78:81], off offset:576
	v_lshl_add_u64 v[82:83], v[82:83], 0, v[164:165]
	v_pk_add_f32 v[76:77], v[76:77], v[140:141]
	v_pk_add_f32 v[80:81], v[88:89], v[152:153]
	v_pk_add_f32 v[78:79], v[86:87], v[150:151]
	v_pk_add_f32 v[74:75], v[74:75], v[138:139]
	v_pk_add_f32 v[68:69], v[68:69], v[132:133]
	v_pk_add_f32 v[66:67], v[66:67], v[130:131]
	v_lshl_add_u64 v[94:95], v[168:169], 0, s[18:19]
	global_store_dwordx4 v[190:191], v[126:129], off
	global_store_dwordx4 v[190:191], v[122:125], off offset:64
	global_store_dwordx4 v[114:115], v[110:113], off
	global_store_dwordx4 v[114:115], v[106:109], off offset:64
	global_store_dwordx4 v[98:99], v[90:93], off offset:64
	global_store_dwordx4 v[82:83], v[78:81], off
	global_store_dwordx4 v[82:83], v[74:77], off offset:64
	global_store_dwordx4 v[82:83], v[70:73], off offset:512
	global_store_dwordx4 v[82:83], v[66:69], off offset:576
	v_lshl_add_u64 v[82:83], v[166:167], 0, v[94:95]
	v_lshl_add_u64 v[70:71], v[166:167], 0, v[96:97]
	v_lshl_add_u64 v[66:67], v[166:167], 0, v[134:135]
	v_lshl_add_u64 v[68:69], v[166:167], 0, v[136:137]
	global_load_dwordx4 v[98:101], v[66:67], off offset:576 nt
	global_load_dwordx4 v[102:105], v[66:67], off offset:512 nt
	global_load_dwordx4 v[106:109], v[66:67], off offset:64 nt
	global_load_dwordx4 v[110:113], v[66:67], off nt
	global_load_dwordx4 v[114:117], v[68:69], off offset:576 nt
	global_load_dwordx4 v[118:121], v[68:69], off offset:512 nt
	global_load_dwordx4 v[122:125], v[68:69], off offset:64 nt
	global_load_dwordx4 v[126:129], v[68:69], off nt
	global_load_dwordx4 v[78:81], v[70:71], off offset:576 nt
	global_load_dwordx4 v[86:89], v[70:71], off offset:512 nt
	global_load_dwordx4 v[90:93], v[70:71], off offset:64 nt
	global_load_dwordx4 v[130:133], v[70:71], off nt
	s_nop 0
	global_load_dwordx4 v[66:69], v[82:83], off offset:576 nt
	global_load_dwordx4 v[70:73], v[82:83], off offset:512 nt
	global_load_dwordx4 v[74:77], v[82:83], off offset:64 nt
	s_nop 0
	global_load_dwordx4 v[82:85], v[82:83], off nt
	s_waitcnt vmcnt(12)
;     __device__ __forceinline__ void operator()(const f32x4 (&acc)[2][2][4][2], const Unit& u, int wr, int wc, int fr, int fq) const {
;     ...
;             for (int m = 0; m < 4; ++m) { const size_t off = (size_t)(row0 + ai * HALF + m * 16) * 1024 + col0;
; #pragma unroll
;                 for (int bj = 0; bj < 2; ++bj)
; #pragma unroll
;                     for (int n = 0; n < 2; ++n) *(f32x4*)(out + off + bj * HALF + n * 16) = xv[m][bj][n] + acc[ai][bj][m][n]; } }
	s_nop 0
	v_pk_add_f32 v[60:61], v[60:61], v[110:111]
	v_lshl_add_u64 v[110:111], s[20:21], 0, v[134:135]
	v_lshl_add_u64 v[110:111], v[110:111], 0, v[164:165]
	v_pk_add_f32 v[50:51], v[50:51], v[104:105]
	v_pk_add_f32 v[48:49], v[48:49], v[102:103]
	s_waitcnt vmcnt(8)
	s_waitcnt vmcnt(4)
	s_waitcnt vmcnt(0)
	global_store_dwordx4 v[110:111], v[48:51], off offset:512
	v_pk_add_f32 v[34:35], v[34:35], v[120:121]
	v_pk_add_f32 v[32:33], v[32:33], v[118:119]
	v_lshl_add_u64 v[48:49], s[20:21], 0, v[136:137]
	v_lshl_add_u64 v[48:49], v[48:49], 0, v[164:165]
	global_store_dwordx4 v[48:49], v[32:35], off offset:512
	v_pk_add_f32 v[18:19], v[18:19], v[88:89]
	v_pk_add_f32 v[16:17], v[16:17], v[86:87]
	v_lshl_add_u64 v[32:33], s[20:21], 0, v[96:97]
	v_lshl_add_u64 v[32:33], v[32:33], 0, v[164:165]
	v_pk_add_f32 v[46:47], v[46:47], v[100:101]
	v_pk_add_f32 v[44:45], v[44:45], v[98:99]
	v_pk_add_f32 v[30:31], v[30:31], v[116:117]
	v_pk_add_f32 v[28:29], v[28:29], v[114:115]
	global_store_dwordx4 v[32:33], v[16:19], off offset:512
	v_pk_add_f32 v[14:15], v[14:15], v[80:81]
	v_pk_add_f32 v[12:13], v[12:13], v[78:79]
	v_lshl_add_u64 v[16:17], s[20:21], 0, v[94:95]
	v_pk_add_f32 v[62:63], v[62:63], v[112:113]
	v_pk_add_f32 v[58:59], v[58:59], v[108:109]
	v_pk_add_f32 v[56:57], v[56:57], v[106:107]
	global_store_dwordx4 v[110:111], v[44:47], off offset:576
	v_pk_add_f32 v[42:43], v[42:43], v[124:125]
	v_pk_add_f32 v[40:41], v[40:41], v[122:123]
	v_pk_add_f32 v[46:47], v[54:55], v[128:129]
	v_pk_add_f32 v[44:45], v[52:53], v[126:127]
	global_store_dwordx4 v[48:49], v[28:31], off offset:576
	v_pk_add_f32 v[26:27], v[26:27], v[92:93]
	v_pk_add_f32 v[24:25], v[24:25], v[90:91]
	v_pk_add_f32 v[30:31], v[38:39], v[132:133]
	v_pk_add_f32 v[28:29], v[36:37], v[130:131]
	global_store_dwordx4 v[32:33], v[12:15], off offset:576
	v_lshl_add_u64 v[16:17], v[16:17], 0, v[164:165]
	v_pk_add_f32 v[10:11], v[10:11], v[76:77]
	v_pk_add_f32 v[14:15], v[22:23], v[84:85]
	v_pk_add_f32 v[12:13], v[20:21], v[82:83]
	v_pk_add_f32 v[8:9], v[8:9], v[74:75]
	v_pk_add_f32 v[6:7], v[6:7], v[72:73]
	v_pk_add_f32 v[4:5], v[4:5], v[70:71]
	v_pk_add_f32 v[2:3], v[2:3], v[68:69]
	v_pk_add_f32 v[0:1], v[0:1], v[66:67]
	s_mov_b64 s[18:19], -1
	global_store_dwordx4 v[110:111], v[60:63], off
	global_store_dwordx4 v[110:111], v[56:59], off offset:64
	global_store_dwordx4 v[48:49], v[44:47], off
	global_store_dwordx4 v[48:49], v[40:43], off offset:64
	global_store_dwordx4 v[32:33], v[28:31], off
	global_store_dwordx4 v[32:33], v[24:27], off offset:64
	global_store_dwordx4 v[16:17], v[12:15], off
	global_store_dwordx4 v[16:17], v[8:11], off offset:64
	global_store_dwordx4 v[16:17], v[4:7], off offset:512
	global_store_dwordx4 v[16:17], v[0:3], off offset:576
	s_cbranch_vccnz .LBB0_2479
	s_andn2_b64 vcc, exec, s[6:7]
	s_cbranch_vccnz .LBB0_2478
	s_barrier
	s_branch .LBB0_2478
